# P7: LayerNorm row statistics of the next unit are loaded without draining vmcnt and converted at first use (plus hoisted U loads)
# baseline (speedup 1.0000x reference)
.LBB0_1026:
	s_cmp_lt_i32 s92, 8
	s_cselect_b64 s[4:5], -1, 0
	s_cmp_gt_i32 s93, 7
	s_cselect_b64 s[6:7], -1, 0
	s_and_b64 s[4:5], s[4:5], s[6:7]
	s_andn2_b64 vcc, exec, s[4:5]
	s_cbranch_vccnz .LBB0_1095
	s_mov_b64 s[4:5], s[0:1]
	s_cmpk_gt_i32 s87, 0xfff
	s_cbranch_scc1 .LBB0_1041
	s_waitcnt vmcnt(0)
	v_mov_b32_e32 v21, 0
	v_mbcnt_lo_u32_b32 v4, -1, 0
	global_load_dwordx4 v[16:19], v21, s[4:5] offset:112
	s_waitcnt lgkmcnt(0)
	global_load_dwordx4 v[0:3], v21, s[4:5] offset:96
	s_and_b32 s4, s3, 0xffffffc0
	v_mbcnt_hi_u32_b32 v4, -1, v4
	v_add_u32_e32 v22, s4, v4
	s_ashr_i32 s4, s87, 4
	s_ashr_i32 s5, s4, 31
	v_lshlrev_b32_e32 v5, 1, v4
	s_lshl_b64 s[6:7], s[4:5], 7
	v_and_b32_e32 v6, 0x7e, v5
	v_ashrrev_i32_e32 v5, 2, v22
	s_add_u32 s16, s70, 0x180000
	v_and_b32_e32 v24, -16, v5
	s_addc_u32 s17, s71, 0
	v_ashrrev_i32_e32 v25, 31, v24
	s_add_u32 s18, s70, 0x42800000
	v_lshl_add_u64 v[8:9], s[6:7], 0, v[24:25]
	s_addc_u32 s19, s71, 0
	v_lshlrev_b64 v[8:9], 12, v[8:9]
	s_lshl_b32 s4, s87, 8
	s_mov_b32 s15, 0
	v_lshl_add_u64 v[8:9], s[18:19], 0, v[8:9]
	s_and_b32 s14, s4, 0xf00
	v_lshl_add_u64 v[8:9], v[8:9], 0, s[14:15]
	v_lshlrev_b32_e32 v26, 1, v6
	v_mov_b32_e32 v27, v21
	v_lshl_add_u64 v[8:9], v[8:9], 0, v[26:27]
	s_movk_i32 s24, 0x2000
	v_add_co_u32_e32 v10, vcc, s24, v8
	s_movk_i32 s25, 0x4000
	s_nop 0
	v_addc_co_u32_e32 v11, vcc, 0, v9, vcc
	v_add_co_u32_e32 v12, vcc, s25, v8
	s_movk_i32 s26, 0x6000
	s_nop 0
	v_addc_co_u32_e32 v13, vcc, 0, v9, vcc
	v_add_co_u32_e32 v14, vcc, s26, v8
	s_mov_b32 s27, 0x8000
	s_nop 0
	v_addc_co_u32_e32 v15, vcc, 0, v9, vcc
	v_add_co_u32_e32 v28, vcc, s27, v8
	s_mov_b32 s28, 0xa000
	s_nop 0
	v_addc_co_u32_e32 v29, vcc, 0, v9, vcc
	global_load_dword v63, v[10:11], off offset:-4096
	global_load_dword v62, v[10:11], off
	global_load_dword v61, v[12:13], off offset:-4096
	global_load_dword v60, v[12:13], off
	global_load_dword v59, v[14:15], off offset:-4096
	global_load_dword v51, v[14:15], off
	global_load_dword v50, v[28:29], off offset:-4096
	global_load_dword v44, v[28:29], off
	v_add_co_u32_e32 v10, vcc, s28, v8
	s_mov_b32 s29, 0xc000
	s_nop 0
	v_addc_co_u32_e32 v11, vcc, 0, v9, vcc
	v_add_co_u32_e32 v12, vcc, s29, v8
	s_mov_b32 s4, 0xd000
	s_nop 0
	v_addc_co_u32_e32 v13, vcc, 0, v9, vcc
	global_load_dword v48, v[10:11], off offset:-4096
	global_load_dword v43, v[10:11], off
	global_load_dword v45, v[12:13], off offset:-4096
	global_load_dword v27, v[12:13], off
	v_add_co_u32_e32 v10, vcc, s4, v8
	s_movk_i32 s4, 0x80
	s_nop 0
	v_addc_co_u32_e32 v11, vcc, 0, v9, vcc
	v_add_co_u32_e32 v12, vcc, 0xe000, v8
	s_mov_b32 s22, -1
	s_nop 0
	v_addc_co_u32_e32 v13, vcc, 0, v9, vcc
	v_add_co_u32_e32 v14, vcc, 0xf000, v8
	v_ashrrev_i32_e32 v23, 31, v22
	s_nop 0
	v_addc_co_u32_e32 v15, vcc, 0, v9, vcc
	global_load_dword v65, v[8:9], off
	global_load_dword v52, v[10:11], off
	global_load_dword v46, v[12:13], off
	global_load_dword v47, v[14:15], off
	v_cmp_gt_i32_e64 s[4:5], s4, v22
	s_movk_i32 s10, 0x1000
	v_mov_b32_e32 v67, 0
	v_mov_b32_e32 v66, 0
	s_and_saveexec_b64 s[8:9], s[4:5]
	s_cbranch_execz .LBB0_1030
	v_lshl_add_u64 v[8:9], s[6:7], 0, v[22:23]
	v_lshl_add_u64 v[8:9], v[8:9], 4, s[16:17]
	global_load_dwordx4 v[124:127], v[8:9], off

.LBB0_1037:
	s_ashr_i32 s56, s2, 4
	s_lshl_b32 s58, s38, 8
	s_ashr_i32 s57, s56, 31
	s_add_u32 s58, s30, s58
	s_addc_u32 s59, s31, 0
	s_lshl_b64 s[56:57], s[56:57], 19
	s_add_u32 s56, s58, s56
	s_addc_u32 s57, s59, s57
	v_mov_b32_e32 v117, v21
	v_mov_b32_e32 v116, v32
	v_lshl_add_u64 v[118:119], s[56:57], 0, v[116:117]
	v_lshl_add_u64 v[118:119], v[118:119], 0, v[34:35]
	v_mov_b32_e32 v116, v36
	v_lshl_add_u64 v[120:121], s[56:57], 0, v[116:117]
	v_lshl_add_u64 v[120:121], v[120:121], 0, v[34:35]
	global_load_dwordx2 v[100:101], v[118:119], off
	global_load_dwordx2 v[102:103], v[118:119], off offset:16
	global_load_dwordx2 v[104:105], v[118:119], off offset:32
	global_load_dwordx2 v[106:107], v[118:119], off offset:48
	global_load_dwordx2 v[108:109], v[120:121], off
	global_load_dwordx2 v[110:111], v[120:121], off offset:16
	global_load_dwordx2 v[112:113], v[120:121], off offset:32
	global_load_dwordx2 v[114:115], v[120:121], off offset:48
	s_and_saveexec_b64 s[10:11], s[4:5]
	s_cbranch_execz .LBB0_1039
	s_waitcnt vmcnt(12)
	v_xor_b32_e32 v4, v124, v125
	v_xor_b32_e32 v6, v126, v127
	v_ffbh_i32_e32 v5, v125
	v_ffbh_i32_e32 v7, v127
	v_ashrrev_i32_e32 v4, 31, v4
	v_ashrrev_i32_e32 v6, 31, v6
	v_add_u32_e32 v5, -1, v5
	v_add_u32_e32 v7, -1, v7
	v_add_u32_e32 v4, 32, v4
	v_add_u32_e32 v6, 32, v6
	v_min_u32_e32 v4, v5, v4
	v_min_u32_e32 v5, v7, v6
	v_lshlrev_b64 v[0:1], v4, v[124:125]
	v_lshlrev_b64 v[2:3], v5, v[126:127]
	v_min_u32_e32 v0, 1, v0
	v_min_u32_e32 v2, 1, v2
	v_or_b32_e32 v0, v1, v0
	v_or_b32_e32 v1, v3, v2
	v_cvt_f32_i32_e32 v0, v0
	v_cvt_f32_i32_e32 v1, v1
	v_sub_u32_e32 v2, 32, v4
	v_sub_u32_e32 v3, 32, v5
	v_ldexp_f32 v0, v0, v2
	v_ldexp_f32 v1, v1, v3
	v_mul_f32_e32 v66, 0x33800000, v0
	v_mul_f32_e32 v67, 0x33800000, v1
	v_mul_f32_e32 v0, 0x3a000000, v66
	v_mul_f32_e32 v1, v0, v0
	v_fma_f32 v1, v67, s36, -v1
	v_max_f32_e32 v1, 0, v1
	v_add_f32_e32 v1, 0x358637bd, v1
	v_mul_f32_e32 v2, 0x4f800000, v1
	v_cmp_gt_f32_e32 vcc, s37, v1
	s_nop 1
	v_cndmask_b32_e32 v1, v1, v2, vcc
	v_sqrt_f32_e32 v2, v1
	s_nop 0
	v_add_u32_e32 v3, -1, v2
	v_fma_f32 v5, -v3, v2, v1
	v_add_u32_e32 v4, 1, v2
	v_cmp_ge_f32_e64 s[8:9], 0, v5
	s_nop 1
	v_cndmask_b32_e64 v3, v2, v3, s[8:9]
	v_fma_f32 v2, -v4, v2, v1
	v_cmp_lt_f32_e64 s[8:9], 0, v2
	s_nop 1
	v_cndmask_b32_e64 v2, v3, v4, s[8:9]
	v_mul_f32_e32 v3, 0x37800000, v2
	v_cndmask_b32_e32 v2, v2, v3, vcc
	v_cmp_class_f32_e32 vcc, v1, v54
	s_nop 1
	v_cndmask_b32_e32 v1, v2, v1, vcc
	v_div_scale_f32 v2, s[8:9], v1, v1, 1.0
	v_rcp_f32_e32 v3, v2
	s_nop 0
	v_fma_f32 v4, -v2, v3, 1.0
	v_fmac_f32_e32 v3, v4, v3
	v_div_scale_f32 v4, vcc, 1.0, v1, 1.0
	v_mul_f32_e32 v5, v4, v3
	v_fma_f32 v6, -v2, v5, v4
	v_fmac_f32_e32 v5, v6, v3
	v_fma_f32 v2, -v2, v5, v4
	v_div_fmas_f32 v2, v2, v3, v5
	v_div_fixup_f32 v1, v2, v1, 1.0
	ds_write_b64 v53, v[0:1]
.LBB0_1039:
	s_or_b64 exec, exec, s[10:11]
	s_waitcnt lgkmcnt(0)
	s_barrier
	ds_read_b128 v[0:3], v55
	s_waitcnt vmcnt(11)
	v_lshlrev_b32_e32 v4, 16, v65
	v_and_b32_e32 v6, 0xffff0000, v65
	v_lshlrev_b32_e32 v5, 16, v63
	v_and_b32_e32 v10, 0xffff0000, v60
	s_waitcnt lgkmcnt(0)
	v_sub_f32_e32 v4, v4, v0
	v_sub_f32_e32 v0, v6, v0
	v_mul_f32_e32 v0, v1, v0
	v_mul_f32_e32 v4, v1, v4
	s_waitcnt vmcnt(10)
	v_fma_f32 v1, v39, v0, v41
	v_and_b32_e32 v0, 0xffff0000, v63
	v_sub_f32_e32 v5, v5, v2
	v_sub_f32_e32 v0, v0, v2
	v_fma_f32 v4, v38, v4, v40
	v_mul_f32_e32 v5, v3, v5
	v_mul_f32_e32 v0, v3, v0
	v_fma_f32 v5, v38, v5, v40
	v_fma_f32 v2, v39, v0, v41
	v_cvt_pk_bf16_f32 v0, v4, v5
	v_cvt_pk_bf16_f32 v4, v1, v2
	ds_read_b128 v[6:9], v55 offset:16
	v_lshlrev_b32_e32 v1, 16, v62
	v_and_b32_e32 v5, 0xffff0000, v61
	v_lshlrev_b32_e32 v2, 16, v61
	v_and_b32_e32 v3, 0xffff0000, v62
	s_waitcnt lgkmcnt(0)
	v_sub_f32_e32 v1, v1, v6
	v_sub_f32_e32 v5, v5, v8
	v_mul_f32_e32 v1, v7, v1
	v_sub_f32_e32 v2, v2, v8
	v_sub_f32_e32 v3, v3, v6
	v_mul_f32_e32 v5, v9, v5
	v_fma_f32 v1, v38, v1, v40
	v_mul_f32_e32 v2, v9, v2
	v_mul_f32_e32 v3, v7, v3
	v_fma_f32 v5, v39, v5, v41
	v_fma_f32 v2, v38, v2, v40
	v_fma_f32 v3, v39, v3, v41
	v_cvt_pk_bf16_f32 v1, v1, v2
	v_cvt_pk_bf16_f32 v5, v3, v5
	ds_read_b128 v[6:9], v55 offset:32
	v_lshlrev_b32_e32 v2, 16, v60
	v_lshlrev_b32_e32 v3, 16, v59
	v_and_b32_e32 v12, 0xffff0000, v51
	v_and_b32_e32 v14, 0xffff0000, v44
	s_waitcnt lgkmcnt(0)
	v_sub_f32_e32 v2, v2, v6
	v_sub_f32_e32 v6, v10, v6
	v_mul_f32_e32 v2, v7, v2
	v_mul_f32_e32 v6, v7, v6
	v_and_b32_e32 v7, 0xffff0000, v59
	v_sub_f32_e32 v3, v3, v8
	v_sub_f32_e32 v7, v7, v8
	v_fma_f32 v2, v38, v2, v40
	v_mul_f32_e32 v3, v9, v3
	v_fma_f32 v6, v39, v6, v41
	v_mul_f32_e32 v7, v9, v7
	v_fma_f32 v3, v38, v3, v40
	v_fma_f32 v7, v39, v7, v41
	v_cvt_pk_bf16_f32 v2, v2, v3
	v_cvt_pk_bf16_f32 v6, v6, v7
	ds_read_b128 v[8:11], v55 offset:48
	v_lshlrev_b32_e32 v3, 16, v51
	v_lshlrev_b32_e32 v7, 16, v50
	v_lshlrev_b32_e32 v13, 16, v48
	v_and_b32_e32 v15, 0xffff0000, v52
	s_waitcnt lgkmcnt(0)
	v_sub_f32_e32 v3, v3, v8
	v_sub_f32_e32 v8, v12, v8
	v_mul_f32_e32 v3, v9, v3
	v_mul_f32_e32 v8, v9, v8
	v_and_b32_e32 v9, 0xffff0000, v50
	v_sub_f32_e32 v7, v7, v10
	v_sub_f32_e32 v9, v9, v10
	v_mul_f32_e32 v7, v11, v7
	v_mul_f32_e32 v9, v11, v9
	v_fma_f32 v3, v38, v3, v40
	v_fma_f32 v7, v38, v7, v40
	v_fma_f32 v8, v39, v8, v41
	v_fma_f32 v9, v39, v9, v41
	v_cvt_pk_bf16_f32 v3, v3, v7
	v_cvt_pk_bf16_f32 v7, v8, v9
	ds_read_b128 v[8:11], v55 offset:64
	v_lshlrev_b32_e32 v12, 16, v44
	s_add_i32 s23, s2, s33
	s_cmpk_gt_i32 s23, 0xfff
	s_cselect_b64 s[8:9], -1, 0
	s_waitcnt lgkmcnt(0)
	v_sub_f32_e32 v12, v12, v8
	v_sub_f32_e32 v8, v14, v8
	v_mul_f32_e32 v8, v9, v8
	v_mul_f32_e32 v12, v9, v12
	v_fma_f32 v9, v39, v8, v41
	v_and_b32_e32 v8, 0xffff0000, v48
	v_sub_f32_e32 v13, v13, v10
	v_sub_f32_e32 v8, v8, v10
	v_fma_f32 v12, v38, v12, v40
	v_mul_f32_e32 v13, v11, v13
	v_mul_f32_e32 v8, v11, v8
	v_fma_f32 v13, v38, v13, v40
	v_fma_f32 v10, v39, v8, v41
	v_cvt_pk_bf16_f32 v8, v12, v13
	v_cvt_pk_bf16_f32 v12, v9, v10
	ds_read_b128 v[60:63], v55 offset:80
	v_lshlrev_b32_e32 v9, 16, v43
	v_and_b32_e32 v13, 0xffff0000, v45
	v_lshlrev_b32_e32 v10, 16, v45
	v_and_b32_e32 v11, 0xffff0000, v43
	s_waitcnt lgkmcnt(0)
	v_sub_f32_e32 v9, v9, v60
	v_sub_f32_e32 v13, v13, v62
	v_mul_f32_e32 v9, v61, v9
	v_sub_f32_e32 v10, v10, v62
	v_sub_f32_e32 v11, v11, v60
	v_mul_f32_e32 v13, v63, v13
	v_fma_f32 v9, v38, v9, v40
	v_mul_f32_e32 v10, v63, v10
	v_mul_f32_e32 v11, v61, v11
	v_fma_f32 v13, v39, v13, v41
	v_fma_f32 v10, v38, v10, v40
	v_fma_f32 v11, v39, v11, v41
	v_cvt_pk_bf16_f32 v9, v9, v10
	v_cvt_pk_bf16_f32 v13, v11, v13
	ds_read_b128 v[60:63], v55 offset:96
	v_lshlrev_b32_e32 v10, 16, v27
	v_and_b32_e32 v14, 0xffff0000, v27
	v_lshlrev_b32_e32 v11, 16, v52
	s_cmpk_lt_i32 s23, 0x1000
	s_waitcnt lgkmcnt(0)
	v_sub_f32_e32 v10, v10, v60
	v_sub_f32_e32 v14, v14, v60
	v_mul_f32_e32 v10, v61, v10
	v_sub_f32_e32 v11, v11, v62
	v_mul_f32_e32 v14, v61, v14
	v_sub_f32_e32 v15, v15, v62
	v_fma_f32 v10, v38, v10, v40
	v_mul_f32_e32 v11, v63, v11
	v_fma_f32 v14, v39, v14, v41
	v_mul_f32_e32 v15, v63, v15
	v_fma_f32 v11, v38, v11, v40
	v_fma_f32 v15, v39, v15, v41
	v_cvt_pk_bf16_f32 v10, v10, v11
	v_cvt_pk_bf16_f32 v14, v14, v15
	ds_read_b128 v[60:63], v55 offset:112
	s_cselect_b32 s14, s23, s2
	s_waitcnt vmcnt(9)
	v_lshlrev_b32_e32 v11, 16, v46
	s_waitcnt vmcnt(8)
	v_lshlrev_b32_e32 v15, 16, v47
	s_ashr_i32 s10, s14, 4
	s_waitcnt lgkmcnt(0)
	v_sub_f32_e32 v11, v11, v60
	v_sub_f32_e32 v15, v15, v62
	v_and_b32_e32 v27, 0xffff0000, v46
	v_and_b32_e32 v33, 0xffff0000, v47
	v_mul_f32_e32 v11, v61, v11
	v_mul_f32_e32 v15, v63, v15
	v_sub_f32_e32 v27, v27, v60
	v_sub_f32_e32 v33, v33, v62
	s_ashr_i32 s11, s10, 31
	v_fma_f32 v11, v38, v11, v40
	v_fma_f32 v15, v38, v15, v40
	v_mul_f32_e32 v27, v61, v27
	v_mul_f32_e32 v33, v63, v33
	s_lshl_b64 s[10:11], s[10:11], 7
	v_fma_f32 v27, v39, v27, v41
	v_fma_f32 v33, v39, v33, v41
	v_cvt_pk_bf16_f32 v11, v11, v15
	v_cvt_pk_bf16_f32 v15, v27, v33
	ds_write_b128 v56, v[0:3] offset:34816
	ds_write_b128 v56, v[8:11] offset:34832
	ds_write_b128 v56, v[4:7] offset:35088
	ds_write_b128 v56, v[12:15] offset:35104
	v_lshl_add_u64 v[0:1], s[10:11], 0, v[24:25]
	v_lshlrev_b64 v[0:1], 12, v[0:1]
	s_lshl_b32 s14, s14, 8
	v_lshl_add_u64 v[0:1], s[18:19], 0, v[0:1]
	s_and_b32 s14, s14, 0xf00
	v_lshl_add_u64 v[0:1], v[0:1], 0, s[14:15]
	v_mov_b32_e32 v27, v21
	v_lshl_add_u64 v[0:1], v[0:1], 0, v[26:27]
	v_add_co_u32_e32 v2, vcc, s24, v0
	s_waitcnt lgkmcnt(0)
	s_barrier
	s_nop 0
	v_addc_co_u32_e32 v3, vcc, 0, v1, vcc
	v_add_co_u32_e32 v4, vcc, s25, v0
	v_mov_b32_e32 v66, 0
	s_nop 0
	v_addc_co_u32_e32 v5, vcc, 0, v1, vcc
	v_add_co_u32_e32 v6, vcc, s26, v0
	v_mov_b32_e32 v67, 0
	s_nop 0
	v_addc_co_u32_e32 v7, vcc, 0, v1, vcc
	v_add_co_u32_e32 v8, vcc, s27, v0
	s_nop 1
	v_addc_co_u32_e32 v9, vcc, 0, v1, vcc
	v_add_co_u32_e32 v10, vcc, s28, v0
	s_nop 1
	v_addc_co_u32_e32 v11, vcc, 0, v1, vcc
	v_add_co_u32_e32 v12, vcc, s29, v0
	s_nop 1
	v_addc_co_u32_e32 v13, vcc, 0, v1, vcc
	global_load_dword v59, v[6:7], off offset:-4096
	global_load_dword v51, v[6:7], off
	global_load_dword v50, v[8:9], off offset:-4096
	global_load_dword v44, v[8:9], off
	global_load_dword v48, v[10:11], off offset:-4096
	global_load_dword v43, v[10:11], off
	global_load_dword v45, v[12:13], off offset:-4096
	global_load_dword v27, v[12:13], off
	v_add_co_u32_e32 v6, vcc, 0xd000, v0
	s_nop 1
	v_addc_co_u32_e32 v7, vcc, 0, v1, vcc
	v_add_co_u32_e32 v8, vcc, 0xe000, v0
	s_nop 1
	v_addc_co_u32_e32 v9, vcc, 0, v1, vcc
	v_add_co_u32_e32 v10, vcc, 0xf000, v0
	s_nop 1
	v_addc_co_u32_e32 v11, vcc, 0, v1, vcc
	global_load_dword v65, v[0:1], off
	global_load_dword v63, v[2:3], off offset:-4096
	global_load_dword v62, v[2:3], off
	global_load_dword v61, v[4:5], off offset:-4096
	global_load_dword v60, v[4:5], off
	global_load_dword v52, v[6:7], off
	global_load_dword v46, v[8:9], off
	global_load_dword v47, v[10:11], off
	s_and_saveexec_b64 s[20:21], s[4:5]
	s_cbranch_execz .LBB0_1031
	v_lshl_add_u64 v[0:1], s[10:11], 0, v[22:23]
	v_lshl_add_u64 v[0:1], v[0:1], 4, s[16:17]
	global_load_dwordx4 v[124:127], v[0:1], off
	s_branch .LBB0_1031
